# v039 + cross-half exchanges out of the common softmax path: update decision on half-row maxima, per-half running sums combined once per unit
# speedup vs baseline: 1.0206x; 1.0206x over previous
; #define PK4(P, BASE, OUT) do { u32x4 w = {cvtpk(P[BASE + 0], P[BASE + 1]), cvtpk(P[BASE + 2], P[BASE + 3]), cvtpk(P[BASE + 4], P[BASE + 5]), cvtpk(P[BASE + 6], P[BASE + 7])}; \
;     OUT = *reinterpret_cast<bf16x8*>(&w); } while (0)
; __device__ __forceinline__ void smax_tile(f32x16& p0, f32x16& p1, float& mhat, float& l_reg, f32x16 (&o)[4], float* al_l, const bool first, int r32, int hi,
;                                           bf16x8& pa0, bf16x8& pa1, bf16x8& pa2, bf16x8& pa3) {
;     ...
; #pragma unroll
;     for (int r = 0; r < 16; ++r) p0[r] = __builtin_amdgcn_exp2f(p0[r]);
; #pragma unroll
;     for (int r = 0; r < 16; ++r) p1[r] = __builtin_amdgcn_exp2f(p1[r]);
;     float ps = p0[0];
; #pragma unroll
;     for (int r = 1; r < 16; ++r) ps += p0[r];
; #pragma unroll
;     for (int r = 0; r < 16; ++r) ps += p1[r];
;     { auto rr = __builtin_amdgcn_permlane32_swap(__float_as_uint(ps), __float_as_uint(ps), false, false); ps = __uint_as_float(rr[0]) + __uint_as_float(rr[1]); }
;     l_reg += ps;
;     ...
;     PK4(p0, 0, pa0); PK4(p0, 8, pa1); PK4(p1, 0, pa2); PK4(p1, 8, pa3);
.LBB0_605:
	v_exp_f32_e32 v96, v96
	v_exp_f32_e32 v97, v97
	v_exp_f32_e32 v98, v98
	v_exp_f32_e32 v99, v99
	v_exp_f32_e32 v100, v100
	v_exp_f32_e32 v101, v101
	v_add_f32_e32 v160, v96, v97
	v_exp_f32_e32 v102, v102
	v_add_f32_e32 v160, v98, v160
	v_exp_f32_e32 v103, v103
	v_add_f32_e32 v160, v99, v160
	v_exp_f32_e32 v104, v104
	v_add_f32_e32 v160, v100, v160
	v_exp_f32_e32 v105, v105
	v_add_f32_e32 v160, v101, v160
	v_exp_f32_e32 v106, v106
	v_add_f32_e32 v160, v102, v160
	v_exp_f32_e32 v107, v107
	v_add_f32_e32 v160, v103, v160
	v_exp_f32_e32 v108, v108
	v_add_f32_e32 v160, v104, v160
	v_exp_f32_e32 v109, v109
	v_add_f32_e32 v160, v105, v160
	v_exp_f32_e32 v110, v110
	v_add_f32_e32 v160, v106, v160
	v_exp_f32_e32 v111, v111
	v_add_f32_e32 v160, v107, v160
	v_exp_f32_e32 v80, v80
	v_add_f32_e32 v160, v108, v160
	v_exp_f32_e32 v81, v81
	v_add_f32_e32 v160, v109, v160
	v_exp_f32_e32 v82, v82
	v_add_f32_e32 v160, v110, v160
	v_exp_f32_e32 v83, v83
	v_add_f32_e32 v160, v111, v160
	v_exp_f32_e32 v84, v84
	v_add_f32_e32 v160, v80, v160
	v_exp_f32_e32 v85, v85
	v_add_f32_e32 v160, v81, v160
	v_exp_f32_e32 v86, v86
	v_add_f32_e32 v160, v82, v160
	v_exp_f32_e32 v87, v87
	v_add_f32_e32 v160, v83, v160
	v_exp_f32_e32 v88, v88
	v_add_f32_e32 v160, v84, v160
	v_exp_f32_e32 v89, v89
	v_add_f32_e32 v160, v85, v160
	v_exp_f32_e32 v90, v90
	v_add_f32_e32 v160, v86, v160
	v_exp_f32_e32 v91, v91
	v_add_f32_e32 v160, v87, v160
	v_exp_f32_e32 v92, v92
	v_add_f32_e32 v160, v88, v160
	v_exp_f32_e32 v93, v93
	v_add_f32_e32 v160, v89, v160
	v_exp_f32_e32 v94, v94
	v_add_f32_e32 v160, v90, v160
	v_exp_f32_e32 v95, v95
	v_add_f32_e32 v160, v91, v160
	v_add_f32_e32 v160, v92, v160
	v_add_f32_e32 v160, v93, v160
	v_add_f32_e32 v160, v94, v160
	v_add_f32_e32 v160, v95, v160
	v_cvt_pk_bf16_f32 v172, v96, v97
	v_cvt_pk_bf16_f32 v173, v98, v99
	v_add_f32_e32 v204, v204, v160
	v_cvt_pk_bf16_f32 v174, v100, v101
	v_cvt_pk_bf16_f32 v175, v102, v103
	v_cvt_pk_bf16_f32 v168, v104, v105
	v_cvt_pk_bf16_f32 v169, v106, v107
	v_cvt_pk_bf16_f32 v170, v108, v109
	v_cvt_pk_bf16_f32 v171, v110, v111
	v_cvt_pk_bf16_f32 v164, v80, v81
	v_cvt_pk_bf16_f32 v165, v82, v83
	v_cvt_pk_bf16_f32 v166, v84, v85
	v_cvt_pk_bf16_f32 v167, v86, v87
	v_cvt_pk_bf16_f32 v160, v88, v89
	v_cvt_pk_bf16_f32 v161, v90, v91
	v_cvt_pk_bf16_f32 v162, v92, v93
	v_cvt_pk_bf16_f32 v163, v94, v95
	s_mul_i32 s47, s26, 0x6000
	s_addk_i32 s93, 0xc000
	s_cmp_lg_u32 s26, 0
	s_cselect_b32 s46, s93, 0x8000
	v_add_u32_e32 v227, s46, v202
	v_add_u32_e32 v207, s47, v185
	v_add_u32_e32 v224, s47, v187
	v_add_u32_e32 v225, s47, v205
	v_add_u32_e32 v226, s47, v206
	s_waitcnt lgkmcnt(0)
	ds_read_b64_tr_b16 v[208:209], v227 offset:0
	ds_read_b64_tr_b16 v[210:211], v227 offset:2048
	ds_read_b64_tr_b16 v[212:213], v227 offset:512
	ds_read_b64_tr_b16 v[214:215], v227 offset:2560
	ds_read_b64_tr_b16 v[216:217], v227 offset:1024
	ds_read_b64_tr_b16 v[218:219], v227 offset:3072
	ds_read_b64_tr_b16 v[220:221], v227 offset:1536
	ds_read_b64_tr_b16 v[222:223], v227 offset:3584
	s_barrier
; #define SBAR() __builtin_amdgcn_sched_barrier(0)
; #define LWN1(a) do { if constexpr (NW == 0) LW1(0, a); else if constexpr (NW == 1) LW1(1, a); else if constexpr (NW == 2) LW1(2, a); else if constexpr (NW == 3) LW1(3, a); else if constexpr (NW == 4) LW1(4, a); else if constexpr (NW == 5) LW1(5, a); else LW1(6, a); } while (0)
; #define LWN2(a, b) do { if constexpr (NW == 0) LW2(0, a, b); else if constexpr (NW == 1) LW2(1, a, b); else if constexpr (NW == 2) LW2(2, a, b); else if constexpr (NW == 3) LW2(3, a, b); else if constexpr (NW == 4) LW2(4, a, b); else if constexpr (NW == 5) LW2(5, a, b); else LW2(6, a, b); } while (0)
; template <int DQK, bool HASQK, bool HASPV, int J> ...
;     constexpr int NQS = HASQK ? 2 * (DQK / 16) : 0, NS = NQS + (HASPV ? 16 : 0);
;     if constexpr (J < NS) {
;         constexpr int rd1 = (J + 1 < NS) ? ((J + 1 < NQS) ? 1 : 2) : 0, rd2 = (J + 2 < NS) ? ((J + 2 < NQS) ? 1 : 2) : 0, rd3 = (J + 3 < NS) ? ((J + 3 < NQS) ? 1 : 2) : 0, NW = rd1 + rd2 + rd3;
;     ...
;         if constexpr (J < NQS) { constexpr int d0 = J >> 1, h = J & 1;
;             LWN1(kf[d0][h]); SBAR();
;             if constexpr (h == 0) p0 = __builtin_amdgcn_mfma_f32_32x32x16_bf16(kf[d0][0], qr[d0], (d0 == 0) ? negm : p0, 0, 0, 0);
;             else p1 = __builtin_amdgcn_mfma_f32_32x32x16_bf16(kf[d0][1], qr[d0], (d0 == 0) ? negm : p1, 0, 0, 0);
;         } else { constexpr int q = J - NQS, g = q >> 2, d = q & 3;
;             LWN2(vf[g][2 * d], vf[g][2 * d + 1]); SBAR();
;             o[d] = __builtin_amdgcn_mfma_f32_32x32x16_bf16(pa[g], (bf16x8){vf[g][2 * d][0], vf[g][2 * d][1], vf[g][2 * d][2], vf[g][2 * d][3], vf[g][2 * d + 1][0], vf[g][2 * d + 1][1], vf[g][2 * d + 1][2], vf[g][2 * d + 1][3]}, o[d], 0, 0, 0);
;         }
;     ...
;         SBAR();
;         slot_read<DQK, HASQK, HASPV, J + 4>(kf, vf, ka_, vb_);
;         SBAR();
;         slot_run<DQK, HASQK, HASPV, J + 1>(kf, vf, ka_, vb_, qr, p0, p1, negm, o, pa);
	s_waitcnt lgkmcnt(6)
	v_mfma_f32_32x32x16_bf16 v[64:79], v[172:175], v[208:211], v[64:79]
	ds_read_b64_tr_b16 v[208:209], v227 offset:4096
	ds_read_b64_tr_b16 v[210:211], v227 offset:6144
	s_waitcnt lgkmcnt(6)
	v_mfma_f32_32x32x16_bf16 v[48:63], v[172:175], v[212:215], v[48:63]
	ds_read_b64_tr_b16 v[212:213], v227 offset:4608
	ds_read_b64_tr_b16 v[214:215], v227 offset:6656
	s_waitcnt lgkmcnt(6)
	v_mfma_f32_32x32x16_bf16 v[32:47], v[172:175], v[216:219], v[32:47]
	ds_read_b64_tr_b16 v[216:217], v227 offset:5120
	ds_read_b64_tr_b16 v[218:219], v227 offset:7168
	s_waitcnt lgkmcnt(6)
	v_mfma_f32_32x32x16_bf16 v[16:31], v[172:175], v[220:223], v[16:31]
	ds_read_b64_tr_b16 v[220:221], v227 offset:5632
	ds_read_b64_tr_b16 v[222:223], v227 offset:7680
	s_waitcnt lgkmcnt(6)
	v_mfma_f32_32x32x16_bf16 v[64:79], v[168:171], v[208:211], v[64:79]
	ds_read_b64_tr_b16 v[208:209], v227 offset:8192
	ds_read_b64_tr_b16 v[210:211], v227 offset:10240
	s_waitcnt lgkmcnt(6)
	v_mfma_f32_32x32x16_bf16 v[48:63], v[168:171], v[212:215], v[48:63]
	ds_read_b64_tr_b16 v[212:213], v227 offset:8704
	ds_read_b64_tr_b16 v[214:215], v227 offset:10752
	s_waitcnt lgkmcnt(6)
	v_mfma_f32_32x32x16_bf16 v[32:47], v[168:171], v[216:219], v[32:47]
	ds_read_b64_tr_b16 v[216:217], v227 offset:9216
	ds_read_b64_tr_b16 v[218:219], v227 offset:11264
	s_waitcnt lgkmcnt(6)
	v_mfma_f32_32x32x16_bf16 v[16:31], v[168:171], v[220:223], v[16:31]
	ds_read_b64_tr_b16 v[220:221], v227 offset:9728
	ds_read_b64_tr_b16 v[222:223], v227 offset:11776
	s_waitcnt lgkmcnt(6)
	v_mfma_f32_32x32x16_bf16 v[64:79], v[164:167], v[208:211], v[64:79]
	ds_read_b64_tr_b16 v[208:209], v227 offset:12288
	ds_read_b64_tr_b16 v[210:211], v227 offset:14336
	s_waitcnt lgkmcnt(6)
	v_mfma_f32_32x32x16_bf16 v[48:63], v[164:167], v[212:215], v[48:63]
	ds_read_b64_tr_b16 v[212:213], v227 offset:12800
	ds_read_b64_tr_b16 v[214:215], v227 offset:14848
	s_waitcnt lgkmcnt(6)
	v_mfma_f32_32x32x16_bf16 v[32:47], v[164:167], v[216:219], v[32:47]
	ds_read_b64_tr_b16 v[216:217], v227 offset:13312
	ds_read_b64_tr_b16 v[218:219], v227 offset:15360
	s_waitcnt lgkmcnt(6)
	v_mfma_f32_32x32x16_bf16 v[16:31], v[164:167], v[220:223], v[16:31]
	ds_read_b64_tr_b16 v[220:221], v227 offset:13824
	ds_read_b64_tr_b16 v[222:223], v227 offset:15872
	v_xor_b32_e32 v80, 0x80000000, v203
	v_mov_b32_e32 v81, v80
	v_mov_b32_e32 v82, v80
	v_mov_b32_e32 v83, v80
	v_mov_b32_e32 v84, v80
	v_mov_b32_e32 v85, v80
	v_mov_b32_e32 v86, v80
	v_mov_b32_e32 v87, v80
	v_mov_b32_e32 v88, v80
	v_mov_b32_e32 v89, v80
	v_mov_b32_e32 v90, v80
	v_mov_b32_e32 v91, v80
	v_mov_b32_e32 v92, v80
	v_mov_b32_e32 v93, v80
	v_mov_b32_e32 v94, v80
	v_mov_b32_e32 v95, v80
	s_waitcnt lgkmcnt(6)
	v_mfma_f32_32x32x16_bf16 v[64:79], v[160:163], v[208:211], v[64:79]
	ds_read_b128 v[208:211], v207 offset:0
	s_waitcnt lgkmcnt(5)
	v_mfma_f32_32x32x16_bf16 v[48:63], v[160:163], v[212:215], v[48:63]
	ds_read_b128 v[212:215], v207 offset:12288
	s_waitcnt lgkmcnt(4)
	v_mfma_f32_32x32x16_bf16 v[32:47], v[160:163], v[216:219], v[32:47]
	ds_read_b128 v[216:219], v224 offset:0
	s_waitcnt lgkmcnt(3)
	v_mfma_f32_32x32x16_bf16 v[16:31], v[160:163], v[220:223], v[16:31]
	ds_read_b128 v[220:223], v224 offset:12288
	s_waitcnt lgkmcnt(3)
	v_mfma_f32_32x32x16_bf16 v[96:111], v[208:211], v[112:115], v[80:95]
	ds_read_b128 v[208:211], v225 offset:0
	s_waitcnt lgkmcnt(3)
	v_mfma_f32_32x32x16_bf16 v[80:95], v[212:215], v[112:115], v[80:95]
	ds_read_b128 v[212:215], v225 offset:12288
	s_waitcnt lgkmcnt(3)
	v_mfma_f32_32x32x16_bf16 v[96:111], v[216:219], v[116:119], v[96:111]
	ds_read_b128 v[216:219], v226 offset:0
	s_waitcnt lgkmcnt(3)
	v_mfma_f32_32x32x16_bf16 v[80:95], v[220:223], v[116:119], v[80:95]
	ds_read_b128 v[220:223], v226 offset:12288
	s_waitcnt lgkmcnt(3)
	v_mfma_f32_32x32x16_bf16 v[96:111], v[208:211], v[120:123], v[96:111]
	ds_read_b128 v[208:211], v207 offset:128
	s_waitcnt lgkmcnt(3)
	v_mfma_f32_32x32x16_bf16 v[80:95], v[212:215], v[120:123], v[80:95]
	ds_read_b128 v[212:215], v207 offset:12416
	s_waitcnt lgkmcnt(3)
	v_mfma_f32_32x32x16_bf16 v[96:111], v[216:219], v[124:127], v[96:111]
	ds_read_b128 v[216:219], v224 offset:128
	s_waitcnt lgkmcnt(3)
	v_mfma_f32_32x32x16_bf16 v[80:95], v[220:223], v[124:127], v[80:95]
	ds_read_b128 v[220:223], v224 offset:12416
	s_waitcnt lgkmcnt(3)
	v_mfma_f32_32x32x16_bf16 v[96:111], v[208:211], v[128:131], v[96:111]
	ds_read_b128 v[208:211], v225 offset:128
	s_waitcnt lgkmcnt(3)
	v_mfma_f32_32x32x16_bf16 v[80:95], v[212:215], v[128:131], v[80:95]
	ds_read_b128 v[212:215], v225 offset:12416
	s_waitcnt lgkmcnt(3)
	v_mfma_f32_32x32x16_bf16 v[96:111], v[216:219], v[132:135], v[96:111]
	ds_read_b128 v[216:219], v226 offset:128
	s_waitcnt lgkmcnt(3)
	v_mfma_f32_32x32x16_bf16 v[80:95], v[220:223], v[132:135], v[80:95]
	ds_read_b128 v[220:223], v226 offset:12416
	s_waitcnt lgkmcnt(3)
	v_mfma_f32_32x32x16_bf16 v[96:111], v[208:211], v[136:139], v[96:111]
	ds_read_b128 v[208:211], v207 offset:256
	s_waitcnt lgkmcnt(3)
	v_mfma_f32_32x32x16_bf16 v[80:95], v[212:215], v[136:139], v[80:95]
	ds_read_b128 v[212:215], v207 offset:12544
	s_waitcnt lgkmcnt(3)
	v_mfma_f32_32x32x16_bf16 v[96:111], v[216:219], v[140:143], v[96:111]
	ds_read_b128 v[216:219], v224 offset:256
	s_waitcnt lgkmcnt(3)
	v_mfma_f32_32x32x16_bf16 v[80:95], v[220:223], v[140:143], v[80:95]
	ds_read_b128 v[220:223], v224 offset:12544
	s_waitcnt lgkmcnt(3)
	v_mfma_f32_32x32x16_bf16 v[96:111], v[208:211], v[144:147], v[96:111]
	ds_read_b128 v[208:211], v225 offset:256
	s_waitcnt lgkmcnt(3)
	v_mfma_f32_32x32x16_bf16 v[80:95], v[212:215], v[144:147], v[80:95]
	ds_read_b128 v[212:215], v225 offset:12544
	s_waitcnt lgkmcnt(3)
	v_mfma_f32_32x32x16_bf16 v[96:111], v[216:219], v[148:151], v[96:111]
	ds_read_b128 v[216:219], v226 offset:256
	s_waitcnt lgkmcnt(3)
	v_mfma_f32_32x32x16_bf16 v[80:95], v[220:223], v[148:151], v[80:95]
	ds_read_b128 v[220:223], v226 offset:12544
	s_waitcnt lgkmcnt(3)
	v_mfma_f32_32x32x16_bf16 v[96:111], v[208:211], v[152:155], v[96:111]
	s_waitcnt lgkmcnt(2)
	v_mfma_f32_32x32x16_bf16 v[80:95], v[212:215], v[152:155], v[80:95]
	s_waitcnt lgkmcnt(1)
	v_mfma_f32_32x32x16_bf16 v[96:111], v[216:219], v[156:159], v[96:111]
	s_waitcnt lgkmcnt(0)
	v_mfma_f32_32x32x16_bf16 v[80:95], v[220:223], v[156:159], v[80:95]
	s_waitcnt vmcnt(0)
	s_waitcnt lgkmcnt(0)
	s_barrier
	s_add_u32 s44, s44, 0x18000
	s_addc_u32 s45, s45, 0
	v_lshl_add_u64 v[194:195], v[194:195], 0, s[28:29]
	s_cmp_eq_u32 s44, 0xbe8000
	v_lshl_add_u64 v[196:197], v[196:197], 0, s[28:29]
	s_cbranch_scc1 .LBB0_616

; __device__ __forceinline__ float vmax3(float x, float y, float z) { float r; asm("v_max3_f32 %0, %1, %2, %3" : "=v"(r) : "v"(x), "v"(y), "v"(z)); return r; }
; __device__ __forceinline__ float vmax2(float x, float y) { float r; asm("v_max_f32 %0, %1, %2" : "=v"(r) : "v"(x), "v"(y)); return r; }
; __device__ __forceinline__ void smax_tile(f32x16& p0, f32x16& p1, float& mhat, float& l_reg, f32x16 (&o)[4], float* al_l, const bool first, int r32, int hi,
;                                           bf16x8& pa0, bf16x8& pa1, bf16x8& pa2, bf16x8& pa3) {
;     float a = vmax3(p0[0], p0[1], p1[0]), b = vmax3(p0[2], p0[3], p1[1]); a = vmax3(a, p1[2], p1[3]);
; #pragma unroll
;     for (int r = 4; r < 16; r += 4) { a = vmax3(a, p0[r], p0[r + 1]); b = vmax3(b, p0[r + 2], p0[r + 3]); a = vmax3(a, p1[r], p1[r + 1]); b = vmax3(b, p1[r + 2], p1[r + 3]); }
;     float rm = vmax2(a, b);
;     { auto rr = __builtin_amdgcn_permlane32_swap(__float_as_uint(rm), __float_as_uint(rm), false, false); rm = vmax2(__uint_as_float(rr[0]), __uint_as_float(rr[1])); }
;     if (__builtin_expect(first || __any(rm > THRL), 0)) {
.LBB0_608:
	s_mov_b32 m0, s47
	v_max3_f32 v160, v96, v97, v80
	global_load_lds_dwordx4 v[194:195], off
	s_add_i32 m0, s47, 0x400
	v_max3_f32 v161, v98, v99, v81
	global_load_lds_dwordx4 v[196:197], off
	v_max3_f32 v160, v160, v82, v83
	v_max3_f32 v161, v161, v102, v103
	v_max3_f32 v160, v160, v100, v101
	v_max3_f32 v161, v161, v86, v87
	v_max3_f32 v160, v160, v84, v85
	v_max3_f32 v161, v161, v106, v107
	v_max3_f32 v160, v160, v104, v105
	v_max3_f32 v161, v161, v90, v91
	v_max3_f32 v160, v160, v88, v89
	v_max3_f32 v161, v161, v110, v111
	v_max3_f32 v160, v160, v108, v109
	v_max3_f32 v161, v161, v94, v95
	v_max3_f32 v160, v160, v92, v93
	v_max_f32 v160, v160, v161
	s_cmp_eq_u32 s44, 0
	s_cbranch_scc1 .Lmy_mh_first
	v_cmp_lt_f32_e32 vcc, s87, v160
	s_cbranch_vccz .LBB0_605
	v_mov_b32_e32 v161, v160
	s_nop 1
	v_permlane32_swap_b32_e32 v160, v161
	v_max_f32_e32 v160, v160, v161
	s_branch .LBB0_614

; __device__ __forceinline__ float vmax2(float x, float y) { float r; asm("v_max_f32 %0, %1, %2" : "=v"(r) : "v"(x), "v"(y)); return r; }
; __device__ __forceinline__ void smax_tile(f32x16& p0, f32x16& p1, float& mhat, float& l_reg, f32x16 (&o)[4], float* al_l, const bool first, int r32, int hi,
;                                           bf16x8& pa0, bf16x8& pa1, bf16x8& pa2, bf16x8& pa3) {
;     ...
;     { auto rr = __builtin_amdgcn_permlane32_swap(__float_as_uint(rm), __float_as_uint(rm), false, false); rm = vmax2(__uint_as_float(rr[0]), __uint_as_float(rr[1])); }
;     if (__builtin_expect(first || __any(rm > THRL), 0)) {
.Lmy_mh_first:
	v_mov_b32_e32 v161, v160
	s_nop 1
	v_permlane32_swap_b32_e32 v160, v161
	v_max_f32_e32 v160, v160, v161
	s_branch .LBB0_615

; #define PK4(P, BASE, OUT) do { u32x4 w = {cvtpk(P[BASE + 0], P[BASE + 1]), cvtpk(P[BASE + 2], P[BASE + 3]), cvtpk(P[BASE + 4], P[BASE + 5]), cvtpk(P[BASE + 6], P[BASE + 7])}; \
;     OUT = *reinterpret_cast<bf16x8*>(&w); } while (0)
; #define DMA_KP(KB, tile, b) do { _Pragma("unroll") for (int _j = 0; _j < NKW; ++_j) glds16((const char*)(KB) + (size_t)(tile) * (KVBLK * LDK * 2) + koff[_j], (LAS unsigned*)(ldsL + (b) * SHM_K + (wid * NKW + _j) * 1024)); } while (0)
; #define DMA_VP(VB, tile, b) do { _Pragma("unroll") for (int _j = 0; _j < 2; ++_j) glds16((const char*)(VB) + (size_t)(tile) * (KVBLK * LDV * 2) + voff[_j], (LAS unsigned*)(ldsL + 3 * SHM_K + (b) * SHM_V + (wid * 2 + _j) * 1024)); } while (0)
; __device__ __forceinline__ void smax_tile(f32x16& p0, f32x16& p1, float& mhat, float& l_reg, f32x16 (&o)[4], float* al_l, const bool first, int r32, int hi,
;                                           bf16x8& pa0, bf16x8& pa1, bf16x8& pa2, bf16x8& pa3) {
;     ...
; #pragma unroll
;     for (int r = 0; r < 16; ++r) p0[r] = __builtin_amdgcn_exp2f(p0[r]);
; #pragma unroll
;     for (int r = 0; r < 16; ++r) p1[r] = __builtin_amdgcn_exp2f(p1[r]);
;     float ps = p0[0];
; #pragma unroll
;     for (int r = 1; r < 16; ++r) ps += p0[r];
; #pragma unroll
;     for (int r = 0; r < 16; ++r) ps += p1[r];
;     { auto rr = __builtin_amdgcn_permlane32_swap(__float_as_uint(ps), __float_as_uint(ps), false, false); ps = __uint_as_float(rr[0]) + __uint_as_float(rr[1]); }
;     l_reg += ps;
;     ...
;     PK4(p0, 0, pa0); PK4(p0, 8, pa1); PK4(p1, 0, pa2); PK4(p1, 8, pa3);
;     ...
;     if (nxt_ && g == 1) { DMA_KP(nKh, 0, 0); DMA_KP(nKh, 1, 1); DMA_VP(nVh, 0, 0); TOUCH_Q(); }
;     SEG_S(NT - 1);
;     if (nxt_ && g == 0) { DMA_KP(nKh, 0, 0); DMA_KP(nKh, 1, 1); DMA_VP(nVh, 0, 0); TOUCH_Q(); }
.LBB0_624:
	v_exp_f32_e32 v96, v96
	v_exp_f32_e32 v97, v97
	v_exp_f32_e32 v98, v98
	v_exp_f32_e32 v99, v99
	v_exp_f32_e32 v100, v100
	v_exp_f32_e32 v101, v101
	v_exp_f32_e32 v123, v108
	v_add_f32_e32 v108, v97, v96
	v_exp_f32_e32 v102, v102
	v_add_f32_e32 v108, v98, v108
	v_exp_f32_e32 v103, v103
	v_add_f32_e32 v108, v99, v108
	v_exp_f32_e32 v104, v104
	v_add_f32_e32 v108, v100, v108
	v_exp_f32_e32 v105, v105
	v_add_f32_e32 v108, v101, v108
	v_exp_f32_e32 v106, v106
	v_add_f32_e32 v108, v102, v108
	v_exp_f32_e32 v107, v107
	v_add_f32_e32 v108, v103, v108
	v_add_f32_e32 v108, v104, v108
	v_exp_f32_e32 v124, v109
	v_add_f32_e32 v108, v105, v108
	v_exp_f32_e32 v125, v110
	v_add_f32_e32 v108, v106, v108
	v_exp_f32_e32 v126, v111
	v_add_f32_e32 v108, v107, v108
	v_exp_f32_e32 v80, v80
	v_add_f32_e32 v108, v123, v108
	v_exp_f32_e32 v81, v81
	v_add_f32_e32 v108, v124, v108
	v_exp_f32_e32 v82, v82
	v_add_f32_e32 v108, v125, v108
	v_exp_f32_e32 v83, v83
	v_add_f32_e32 v108, v126, v108
	v_exp_f32_e32 v84, v84
	v_add_f32_e32 v108, v80, v108
	v_exp_f32_e32 v85, v85
	v_add_f32_e32 v108, v81, v108
	v_exp_f32_e32 v86, v86
	v_add_f32_e32 v108, v82, v108
	v_exp_f32_e32 v87, v87
	v_add_f32_e32 v108, v83, v108
	v_exp_f32_e32 v88, v88
	v_add_f32_e32 v108, v84, v108
	v_exp_f32_e32 v89, v89
	v_add_f32_e32 v108, v85, v108
	v_exp_f32_e32 v90, v90
	v_add_f32_e32 v108, v86, v108
	v_exp_f32_e32 v91, v91
	v_add_f32_e32 v108, v87, v108
	v_exp_f32_e32 v92, v92
	v_add_f32_e32 v108, v88, v108
	v_exp_f32_e32 v93, v93
	v_add_f32_e32 v108, v89, v108
	v_exp_f32_e32 v94, v94
	v_add_f32_e32 v108, v90, v108
	v_exp_f32_e32 v95, v95
	v_add_f32_e32 v108, v91, v108
	v_add_f32_e32 v108, v92, v108
	v_add_f32_e32 v108, v93, v108
	v_add_f32_e32 v108, v94, v108
	v_add_f32_e32 v108, v95, v108
	v_add_f32_e32 v122, v204, v108
	v_cvt_pk_bf16_f32 v108, v96, v97
	v_cvt_pk_bf16_f32 v109, v98, v99
	v_cvt_pk_bf16_f32 v110, v100, v101
	v_cvt_pk_bf16_f32 v111, v102, v103
	v_cvt_pk_bf16_f32 v104, v104, v105
	v_cvt_pk_bf16_f32 v105, v106, v107
	v_cvt_pk_bf16_f32 v106, v123, v124
	v_cvt_pk_bf16_f32 v107, v125, v126
	v_cvt_pk_bf16_f32 v100, v80, v81
	v_cvt_pk_bf16_f32 v101, v82, v83
	v_cvt_pk_bf16_f32 v102, v84, v85
	v_cvt_pk_bf16_f32 v103, v86, v87
	v_cvt_pk_bf16_f32 v96, v88, v89
	v_cvt_pk_bf16_f32 v97, v90, v91
	v_cvt_pk_bf16_f32 v98, v92, v93
	v_cvt_pk_bf16_f32 v99, v94, v95
	s_cmp_eq_u32 s92, 0
	s_cselect_b64 s[38:39], -1, 0
	s_waitcnt lgkmcnt(0)
	s_barrier
	s_and_b64 s[42:43], s[44:45], s[38:39]
	s_andn2_b64 vcc, exec, s[42:43]
	s_cbranch_vccnz .LBB0_631
	s_add_i32 s42, s73, 0
	s_mov_b32 m0, s42
	s_add_i32 s43, s74, 0
	s_add_i32 s44, s75, 0
	global_load_lds_dwordx4 v[120:121], off
	s_mov_b32 m0, s43
	s_add_u32 s36, s36, 0x18000
	global_load_lds_dwordx4 v[118:119], off
	s_mov_b32 m0, s44
	s_addc_u32 s37, s37, 0
	global_load_lds_dwordx4 v[116:117], off
	v_lshl_add_u64 v[80:81], s[36:37], 0, v[178:179]
	s_add_i32 m0, s42, 0x6000
	s_nop 0
	global_load_lds_dwordx4 v[80:81], off
	v_lshl_add_u64 v[80:81], s[36:37], 0, v[180:181]
	s_add_i32 m0, s43, 0x6000
	s_nop 0
	global_load_lds_dwordx4 v[80:81], off
	v_lshl_add_u64 v[80:81], s[36:37], 0, v[182:183]
	s_add_i32 m0, s44, 0x6000
	s_nop 0
	global_load_lds_dwordx4 v[80:81], off
	s_mov_b32 m0, s76
	s_nop 0
	global_load_lds_dwordx4 v[114:115], off
	s_add_i32 m0, s76, 0x400
	s_cmp_eq_u64 s[34:35], 0
	global_load_lds_dwordx4 v[112:113], off
	s_cbranch_scc1 .LBB0_631
	v_cmp_gt_i32_e32 vcc, s86, v200
	s_and_saveexec_b64 s[36:37], vcc
	s_cbranch_execz .LBB0_628
	v_mul_hi_i32 v80, v200, s88
	v_lshrrev_b32_e32 v81, 31, v80
	v_add_u32_e32 v82, v80, v81
	v_add_u32_e32 v83, s57, v82
	v_lshl_add_u32 v82, v82, 1, v82
	v_sub_u32_e32 v82, v200, v82
	v_mov_b64_e32 v[80:81], s[34:35]
	v_lshlrev_b32_e32 v82, 7, v82
	v_mad_i64_i32 v[80:81], s[42:43], v83, s83, v[80:81]
	v_ashrrev_i32_e32 v83, 31, v82
	v_lshl_add_u64 v[80:81], v[80:81], 0, v[82:83]
	s_add_i32 m0, s66, 0x1f000
	s_nop 0
	global_load_lds_dword v[80:81], off

; #define SBAR() __builtin_amdgcn_sched_barrier(0)
; #define LWN1(a) do { if constexpr (NW == 0) LW1(0, a); else if constexpr (NW == 1) LW1(1, a); else if constexpr (NW == 2) LW1(2, a); else if constexpr (NW == 3) LW1(3, a); else if constexpr (NW == 4) LW1(4, a); else if constexpr (NW == 5) LW1(5, a); else LW1(6, a); } while (0)
; #define LWN2(a, b) do { if constexpr (NW == 0) LW2(0, a, b); else if constexpr (NW == 1) LW2(1, a, b); else if constexpr (NW == 2) LW2(2, a, b); else if constexpr (NW == 3) LW2(3, a, b); else if constexpr (NW == 4) LW2(4, a, b); else if constexpr (NW == 5) LW2(5, a, b); else LW2(6, a, b); } while (0)
; __device__ __forceinline__ void smax_tile(f32x16& p0, f32x16& p1, float& mhat, float& l_reg, f32x16 (&o)[4], float* al_l, const bool first, int r32, int hi,
;                                           bf16x8& pa0, bf16x8& pa1, bf16x8& pa2, bf16x8& pa3) {
;     ...
;     { auto rr = __builtin_amdgcn_permlane32_swap(__float_as_uint(ps), __float_as_uint(ps), false, false); ps = __uint_as_float(rr[0]) + __uint_as_float(rr[1]); }
;     l_reg += ps;
; template <int DQK, bool HASQK, bool HASPV, int J> ...
;     constexpr int NQS = HASQK ? 2 * (DQK / 16) : 0, NS = NQS + (HASPV ? 16 : 0);
;     if constexpr (J < NS) {
;         constexpr int rd1 = (J + 1 < NS) ? ((J + 1 < NQS) ? 1 : 2) : 0, rd2 = (J + 2 < NS) ? ((J + 2 < NQS) ? 1 : 2) : 0, rd3 = (J + 3 < NS) ? ((J + 3 < NQS) ? 1 : 2) : 0, NW = rd1 + rd2 + rd3;
;     ...
;         if constexpr (J < NQS) { constexpr int d0 = J >> 1, h = J & 1;
;             LWN1(kf[d0][h]); SBAR();
;             if constexpr (h == 0) p0 = __builtin_amdgcn_mfma_f32_32x32x16_bf16(kf[d0][0], qr[d0], (d0 == 0) ? negm : p0, 0, 0, 0);
;             else p1 = __builtin_amdgcn_mfma_f32_32x32x16_bf16(kf[d0][1], qr[d0], (d0 == 0) ? negm : p1, 0, 0, 0);
;         } else { constexpr int q = J - NQS, g = q >> 2, d = q & 3;
;             LWN2(vf[g][2 * d], vf[g][2 * d + 1]); SBAR();
;             o[d] = __builtin_amdgcn_mfma_f32_32x32x16_bf16(pa[g], (bf16x8){vf[g][2 * d][0], vf[g][2 * d][1], vf[g][2 * d][2], vf[g][2 * d][3], vf[g][2 * d + 1][0], vf[g][2 * d + 1][1], vf[g][2 * d + 1][2], vf[g][2 * d + 1][3]}, o[d], 0, 0, 0);
;         }
;     ...
;         SBAR();
;         slot_read<DQK, HASQK, HASPV, J + 4>(kf, vf, ka_, vb_);
;         SBAR();
;         slot_run<DQK, HASQK, HASPV, J + 1>(kf, vf, ka_, vb_, qr, p0, p1, negm, o, pa);
.LBB0_631:
	s_add_i32 s34, s26, 1
	s_cmp_lg_u32 s26, 2
	s_cselect_b32 s26, s34, 0
	s_lshl_b32 s34, s26, 14
	s_addk_i32 s34, 0xc000
	s_cmp_lg_u32 s26, 0
	s_cselect_b32 s26, s34, 0x8000
	v_add_u32_e32 v120, s26, v202
	ds_read_b64_tr_b16 v[112:113], v120 offset:0
	ds_read_b64_tr_b16 v[114:115], v120 offset:0x800
	ds_read_b64_tr_b16 v[116:117], v120 offset:0x200
	ds_read_b64_tr_b16 v[118:119], v120 offset:0xa00
	ds_read_b64_tr_b16 v[124:125], v120 offset:0x400
	ds_read_b64_tr_b16 v[126:127], v120 offset:0xc00
	ds_read_b64_tr_b16 v[128:129], v120 offset:0x600
	ds_read_b64_tr_b16 v[130:131], v120 offset:0xe00
	v_xor_b32_e32 v80, 0x80000000, v203
	v_mov_b32_e32 v81, v80
	v_mov_b32_e32 v82, v80
	v_mov_b32_e32 v83, v80
	v_mov_b32_e32 v84, v80
	v_mov_b32_e32 v85, v80
	v_mov_b32_e32 v86, v80
	v_mov_b32_e32 v87, v80
	v_mov_b32_e32 v88, v80
	v_mov_b32_e32 v89, v80
	v_mov_b32_e32 v90, v80
	v_mov_b32_e32 v91, v80
	v_mov_b32_e32 v92, v80
	v_mov_b32_e32 v93, v80
	v_mov_b32_e32 v94, v80
	v_mov_b32_e32 v95, v80
	s_waitcnt lgkmcnt(6)
	s_nop 0
	v_mfma_f32_32x32x16_bf16 v[64:79], v[108:111], v[112:115], v[64:79]
	ds_read_b64_tr_b16 v[80:81], v120 offset:0x1000
	ds_read_b64_tr_b16 v[82:83], v120 offset:0x1800
	s_waitcnt lgkmcnt(6)
	s_nop 0
	v_mfma_f32_32x32x16_bf16 v[48:63], v[108:111], v[116:119], v[48:63]
	ds_read_b64_tr_b16 v[84:85], v120 offset:0x1200
	ds_read_b64_tr_b16 v[86:87], v120 offset:0x1a00
	s_waitcnt lgkmcnt(6)
	s_nop 0
	v_mfma_f32_32x32x16_bf16 v[32:47], v[108:111], v[124:127], v[32:47]
	ds_read_b64_tr_b16 v[88:89], v120 offset:0x1400
	ds_read_b64_tr_b16 v[90:91], v120 offset:0x1c00
	s_waitcnt lgkmcnt(6)
	s_nop 0
	v_mfma_f32_32x32x16_bf16 v[16:31], v[108:111], v[128:131], v[16:31]
	ds_read_b64_tr_b16 v[92:93], v120 offset:0x1600
	ds_read_b64_tr_b16 v[94:95], v120 offset:0x1e00
	s_waitcnt lgkmcnt(6)
	s_nop 0
	v_mfma_f32_32x32x16_bf16 v[64:79], v[104:107], v[80:83], v[64:79]
	ds_read_b64_tr_b16 v[80:81], v120 offset:0x2000
	ds_read_b64_tr_b16 v[82:83], v120 offset:0x2800
	s_waitcnt lgkmcnt(6)
	s_nop 0
	v_mfma_f32_32x32x16_bf16 v[48:63], v[104:107], v[84:87], v[48:63]
	ds_read_b64_tr_b16 v[84:85], v120 offset:0x2200
	ds_read_b64_tr_b16 v[86:87], v120 offset:0x2a00
	s_waitcnt lgkmcnt(6)
	s_nop 0
	v_mfma_f32_32x32x16_bf16 v[32:47], v[104:107], v[88:91], v[32:47]
	ds_read_b64_tr_b16 v[88:89], v120 offset:0x2400
	ds_read_b64_tr_b16 v[90:91], v120 offset:0x2c00
	s_waitcnt lgkmcnt(6)
	s_nop 0
	v_mfma_f32_32x32x16_bf16 v[16:31], v[104:107], v[92:95], v[16:31]
	ds_read_b64_tr_b16 v[92:93], v120 offset:0x2600
	ds_read_b64_tr_b16 v[94:95], v120 offset:0x2e00
	s_waitcnt lgkmcnt(6)
	s_nop 0
	v_mfma_f32_32x32x16_bf16 v[64:79], v[100:103], v[80:83], v[64:79]
	ds_read_b64_tr_b16 v[80:81], v120 offset:0x3000
	ds_read_b64_tr_b16 v[82:83], v120 offset:0x3800
	s_waitcnt lgkmcnt(6)
	s_nop 0
	v_mfma_f32_32x32x16_bf16 v[48:63], v[100:103], v[84:87], v[48:63]
	ds_read_b64_tr_b16 v[84:85], v120 offset:0x3200
	ds_read_b64_tr_b16 v[86:87], v120 offset:0x3a00
	s_waitcnt lgkmcnt(6)
	s_nop 0
	v_mfma_f32_32x32x16_bf16 v[32:47], v[100:103], v[88:91], v[32:47]
	ds_read_b64_tr_b16 v[88:89], v120 offset:0x3400
	ds_read_b64_tr_b16 v[90:91], v120 offset:0x3c00
	s_waitcnt lgkmcnt(6)
	s_nop 0
	v_mfma_f32_32x32x16_bf16 v[16:31], v[100:103], v[92:95], v[16:31]
	ds_read_b64_tr_b16 v[92:93], v120 offset:0x3600
	ds_read_b64_tr_b16 v[94:95], v120 offset:0x3e00
	s_waitcnt lgkmcnt(6)
	s_nop 0
	v_mfma_f32_32x32x16_bf16 v[64:79], v[96:99], v[80:83], v[64:79]
	s_waitcnt lgkmcnt(4)
	s_nop 0
	v_mfma_f32_32x32x16_bf16 v[48:63], v[96:99], v[84:87], v[48:63]
	s_waitcnt lgkmcnt(2)
	s_nop 0
	v_mfma_f32_32x32x16_bf16 v[32:47], v[96:99], v[88:91], v[32:47]
	s_waitcnt lgkmcnt(0)
	s_nop 0
	v_mfma_f32_32x32x16_bf16 v[16:31], v[96:99], v[92:95], v[16:31]
	s_waitcnt lgkmcnt(0)
	s_barrier
	v_mov_b32_e32 v244, v122
	s_nop 1
	v_permlane32_swap_b32_e32 v122, v244
	v_add_f32_e32 v122, v122, v244
	s_andn2_b64 vcc, exec, s[38:39]
	s_cbranch_vccz .LBB0_633
	s_and_saveexec_b64 s[34:35], s[10:11]
	s_cbranch_execz .LBB0_593
	s_branch .LBB0_634

; #define PK4(P, BASE, OUT) do { u32x4 w = {cvtpk(P[BASE + 0], P[BASE + 1]), cvtpk(P[BASE + 2], P[BASE + 3]), cvtpk(P[BASE + 4], P[BASE + 5]), cvtpk(P[BASE + 6], P[BASE + 7])}; \
;     OUT = *reinterpret_cast<bf16x8*>(&w); } while (0)
; __device__ __forceinline__ void smax_tile(f32x16& p0, f32x16& p1, float& mhat, float& l_reg, f32x16 (&o)[4], float* al_l, const bool first, int r32, int hi,
;                                           bf16x8& pa0, bf16x8& pa1, bf16x8& pa2, bf16x8& pa3) {
;     ...
; #pragma unroll
;     for (int r = 0; r < 16; ++r) p0[r] = __builtin_amdgcn_exp2f(p0[r]);
; #pragma unroll
;     for (int r = 0; r < 16; ++r) p1[r] = __builtin_amdgcn_exp2f(p1[r]);
;     float ps = p0[0];
; #pragma unroll
;     for (int r = 1; r < 16; ++r) ps += p0[r];
; #pragma unroll
;     for (int r = 0; r < 16; ++r) ps += p1[r];
;     { auto rr = __builtin_amdgcn_permlane32_swap(__float_as_uint(ps), __float_as_uint(ps), false, false); ps = __uint_as_float(rr[0]) + __uint_as_float(rr[1]); }
;     l_reg += ps;
;     ...
;     PK4(p0, 0, pa0); PK4(p0, 8, pa1); PK4(p1, 0, pa2); PK4(p1, 8, pa3);
.LBB0_651:
	v_exp_f32_e32 v96, v96
	v_exp_f32_e32 v97, v97
	v_exp_f32_e32 v98, v98
	v_exp_f32_e32 v99, v99
	v_exp_f32_e32 v100, v100
	v_exp_f32_e32 v101, v101
	v_add_f32_e32 v128, v96, v97
	v_exp_f32_e32 v102, v102
	v_add_f32_e32 v128, v98, v128
	v_exp_f32_e32 v103, v103
	v_add_f32_e32 v128, v99, v128
	v_exp_f32_e32 v104, v104
	v_add_f32_e32 v128, v100, v128
	v_exp_f32_e32 v105, v105
	v_add_f32_e32 v128, v101, v128
	v_exp_f32_e32 v106, v106
	v_add_f32_e32 v128, v102, v128
	v_exp_f32_e32 v107, v107
	v_add_f32_e32 v128, v103, v128
	v_exp_f32_e32 v108, v108
	v_add_f32_e32 v128, v104, v128
	v_exp_f32_e32 v109, v109
	v_add_f32_e32 v128, v105, v128
	v_exp_f32_e32 v110, v110
	v_add_f32_e32 v128, v106, v128
	v_exp_f32_e32 v111, v111
	v_add_f32_e32 v128, v107, v128
	v_exp_f32_e32 v80, v80
	v_add_f32_e32 v128, v108, v128
	v_exp_f32_e32 v81, v81
	v_add_f32_e32 v128, v109, v128
	v_exp_f32_e32 v82, v82
	v_add_f32_e32 v128, v110, v128
	v_exp_f32_e32 v83, v83
	v_add_f32_e32 v128, v111, v128
	v_exp_f32_e32 v84, v84
	v_add_f32_e32 v128, v80, v128
	v_exp_f32_e32 v85, v85
	v_add_f32_e32 v128, v81, v128
	v_exp_f32_e32 v86, v86
	v_add_f32_e32 v128, v82, v128
	v_exp_f32_e32 v87, v87
	v_add_f32_e32 v128, v83, v128
	v_exp_f32_e32 v88, v88
	v_add_f32_e32 v128, v84, v128
	v_exp_f32_e32 v89, v89
	v_add_f32_e32 v128, v85, v128
	v_exp_f32_e32 v90, v90
	v_add_f32_e32 v128, v86, v128
	v_exp_f32_e32 v91, v91
	v_add_f32_e32 v128, v87, v128
	v_exp_f32_e32 v92, v92
	v_add_f32_e32 v128, v88, v128
	v_exp_f32_e32 v93, v93
	v_add_f32_e32 v128, v89, v128
	v_exp_f32_e32 v94, v94
	v_add_f32_e32 v128, v90, v128
	v_exp_f32_e32 v95, v95
	v_add_f32_e32 v128, v91, v128
	v_add_f32_e32 v128, v92, v128
	v_add_f32_e32 v128, v93, v128
	v_add_f32_e32 v128, v94, v128
	v_add_f32_e32 v128, v95, v128
	v_cvt_pk_bf16_f32 v162, v96, v97
	v_cvt_pk_bf16_f32 v163, v98, v99
	v_add_f32_e32 v159, v159, v128
	v_cvt_pk_bf16_f32 v164, v100, v101
	v_cvt_pk_bf16_f32 v165, v102, v103
	v_cvt_pk_bf16_f32 v166, v104, v105
	v_cvt_pk_bf16_f32 v167, v106, v107
	v_cvt_pk_bf16_f32 v168, v108, v109
	v_cvt_pk_bf16_f32 v169, v110, v111
	v_cvt_pk_bf16_f32 v132, v80, v81
	v_cvt_pk_bf16_f32 v133, v82, v83
	v_cvt_pk_bf16_f32 v134, v84, v85
	v_cvt_pk_bf16_f32 v135, v86, v87
	v_cvt_pk_bf16_f32 v128, v88, v89
	v_cvt_pk_bf16_f32 v129, v90, v91
	v_cvt_pk_bf16_f32 v130, v92, v93
	v_cvt_pk_bf16_f32 v131, v94, v95
	s_cmp_lg_u32 s86, 0
	s_waitcnt lgkmcnt(0)
	s_barrier
; #define SBAR() __builtin_amdgcn_sched_barrier(0)
; #define LWN1(a) do { if constexpr (NW == 0) LW1(0, a); else if constexpr (NW == 1) LW1(1, a); else if constexpr (NW == 2) LW1(2, a); else if constexpr (NW == 3) LW1(3, a); else if constexpr (NW == 4) LW1(4, a); else if constexpr (NW == 5) LW1(5, a); else LW1(6, a); } while (0)
; #define LWN2(a, b) do { if constexpr (NW == 0) LW2(0, a, b); else if constexpr (NW == 1) LW2(1, a, b); else if constexpr (NW == 2) LW2(2, a, b); else if constexpr (NW == 3) LW2(3, a, b); else if constexpr (NW == 4) LW2(4, a, b); else if constexpr (NW == 5) LW2(5, a, b); else LW2(6, a, b); } while (0)
; template <int DQK, bool HASQK, bool HASPV, int J> ...
;     constexpr int NQS = HASQK ? 2 * (DQK / 16) : 0, NS = NQS + (HASPV ? 16 : 0);
;     if constexpr (J < NS) {
;         constexpr int rd1 = (J + 1 < NS) ? ((J + 1 < NQS) ? 1 : 2) : 0, rd2 = (J + 2 < NS) ? ((J + 2 < NQS) ? 1 : 2) : 0, rd3 = (J + 3 < NS) ? ((J + 3 < NQS) ? 1 : 2) : 0, NW = rd1 + rd2 + rd3;
;     ...
;         if constexpr (J < NQS) { constexpr int d0 = J >> 1, h = J & 1;
;             LWN1(kf[d0][h]); SBAR();
;             if constexpr (h == 0) p0 = __builtin_amdgcn_mfma_f32_32x32x16_bf16(kf[d0][0], qr[d0], (d0 == 0) ? negm : p0, 0, 0, 0);
;             else p1 = __builtin_amdgcn_mfma_f32_32x32x16_bf16(kf[d0][1], qr[d0], (d0 == 0) ? negm : p1, 0, 0, 0);
;         } else { constexpr int q = J - NQS, g = q >> 2, d = q & 3;
;             LWN2(vf[g][2 * d], vf[g][2 * d + 1]); SBAR();
;             o[d] = __builtin_amdgcn_mfma_f32_32x32x16_bf16(pa[g], (bf16x8){vf[g][2 * d][0], vf[g][2 * d][1], vf[g][2 * d][2], vf[g][2 * d][3], vf[g][2 * d + 1][0], vf[g][2 * d + 1][1], vf[g][2 * d + 1][2], vf[g][2 * d + 1][3]}, o[d], 0, 0, 0);
;         }
;     ...
;         SBAR();
;         slot_read<DQK, HASQK, HASPV, J + 4>(kf, vf, ka_, vb_);
;         SBAR();
;         slot_run<DQK, HASQK, HASPV, J + 1>(kf, vf, ka_, vb_, qr, p0, p1, negm, o, pa);
	s_cselect_b32 s46, s87, 0x8000
	s_lshl_b32 s47, s86, 13
	v_add_u32_e32 v81, s47, v141
	v_add_u32_e32 v82, s47, v143
	ds_read_b128 v[170:173], v81 offset:0
	ds_read_b128 v[174:177], v81 offset:0x1000
	ds_read_b128 v[178:181], v82 offset:0
	ds_read_b128 v[182:185], v82 offset:0x1000
	v_xor_b32_e32 v80, 0x80000000, v158
	v_add_u32_e32 v186, s47, v160
	v_add_u32_e32 v187, s47, v161
	v_add_u32_e32 v188, s46, v157
	v_mov_b32_e32 v81, v80
	v_mov_b32_e32 v82, v80
	v_mov_b32_e32 v83, v80
	v_mov_b32_e32 v84, v80
	v_mov_b32_e32 v85, v80
	v_mov_b32_e32 v86, v80
	v_mov_b32_e32 v87, v80
	v_mov_b32_e32 v88, v80
	v_mov_b32_e32 v89, v80
	v_mov_b32_e32 v90, v80
	v_mov_b32_e32 v91, v80
	v_mov_b32_e32 v92, v80
	v_mov_b32_e32 v93, v80
	v_mov_b32_e32 v94, v80
	v_mov_b32_e32 v95, v80
	s_waitcnt lgkmcnt(3)
	s_nop 1
	v_mfma_f32_32x32x16_bf16 v[96:111], v[170:173], v[112:115], v[80:95]
	ds_read_b128 v[170:173], v186 offset:0
	s_waitcnt lgkmcnt(3)
	s_nop 0
	v_mfma_f32_32x32x16_bf16 v[80:95], v[174:177], v[112:115], v[80:95]
	ds_read_b128 v[174:177], v186 offset:0x1000
	s_waitcnt lgkmcnt(3)
	s_nop 0
	v_mfma_f32_32x32x16_bf16 v[96:111], v[178:181], v[116:119], v[96:111]
	ds_read_b128 v[178:181], v187 offset:0
	s_waitcnt lgkmcnt(3)
	s_nop 0
	v_mfma_f32_32x32x16_bf16 v[80:95], v[182:185], v[116:119], v[80:95]
	ds_read_b128 v[182:185], v187 offset:0x1000
	s_waitcnt lgkmcnt(3)
	s_nop 0
	v_mfma_f32_32x32x16_bf16 v[96:111], v[170:173], v[120:123], v[96:111]
	ds_read_b64_tr_b16 v[170:171], v188 offset:0
	ds_read_b64_tr_b16 v[172:173], v188 offset:0x800
	s_waitcnt lgkmcnt(4)
	s_nop 0
	v_mfma_f32_32x32x16_bf16 v[80:95], v[174:177], v[120:123], v[80:95]
	ds_read_b64_tr_b16 v[174:175], v188 offset:0x200
	ds_read_b64_tr_b16 v[176:177], v188 offset:0xa00
	s_waitcnt lgkmcnt(5)
	s_nop 0
	v_mfma_f32_32x32x16_bf16 v[96:111], v[178:181], v[124:127], v[96:111]
	ds_read_b64_tr_b16 v[178:179], v188 offset:0x400
	ds_read_b64_tr_b16 v[180:181], v188 offset:0xc00
	s_waitcnt lgkmcnt(6)
	s_nop 0
	v_mfma_f32_32x32x16_bf16 v[80:95], v[182:185], v[124:127], v[80:95]
	ds_read_b64_tr_b16 v[182:183], v188 offset:0x600
	ds_read_b64_tr_b16 v[184:185], v188 offset:0xe00
	s_waitcnt lgkmcnt(6)
	s_nop 0
	v_mfma_f32_32x32x16_bf16 v[64:79], v[162:165], v[170:173], v[64:79]
	ds_read_b64_tr_b16 v[170:171], v188 offset:0x1000
	ds_read_b64_tr_b16 v[172:173], v188 offset:0x1800
	s_waitcnt lgkmcnt(6)
	s_nop 0
	v_mfma_f32_32x32x16_bf16 v[48:63], v[162:165], v[174:177], v[48:63]
	ds_read_b64_tr_b16 v[174:175], v188 offset:0x1200
	ds_read_b64_tr_b16 v[176:177], v188 offset:0x1a00
	s_waitcnt lgkmcnt(6)
	s_nop 0
	v_mfma_f32_32x32x16_bf16 v[32:47], v[162:165], v[178:181], v[32:47]
	ds_read_b64_tr_b16 v[178:179], v188 offset:0x1400
	ds_read_b64_tr_b16 v[180:181], v188 offset:0x1c00
	s_waitcnt lgkmcnt(6)
	s_nop 0
	v_mfma_f32_32x32x16_bf16 v[16:31], v[162:165], v[182:185], v[16:31]
	ds_read_b64_tr_b16 v[162:163], v188 offset:0x1600
	ds_read_b64_tr_b16 v[164:165], v188 offset:0x1e00
	s_waitcnt lgkmcnt(6)
	s_nop 0
	v_mfma_f32_32x32x16_bf16 v[64:79], v[166:169], v[170:173], v[64:79]
	ds_read_b64_tr_b16 v[170:171], v188 offset:0x2000
	ds_read_b64_tr_b16 v[172:173], v188 offset:0x2800
	s_waitcnt lgkmcnt(6)
	s_nop 0
	v_mfma_f32_32x32x16_bf16 v[48:63], v[166:169], v[174:177], v[48:63]
	ds_read_b64_tr_b16 v[174:175], v188 offset:0x2200
	ds_read_b64_tr_b16 v[176:177], v188 offset:0x2a00
	s_waitcnt lgkmcnt(6)
	s_nop 0
	v_mfma_f32_32x32x16_bf16 v[32:47], v[166:169], v[178:181], v[32:47]
	ds_read_b64_tr_b16 v[178:179], v188 offset:0x2400
	ds_read_b64_tr_b16 v[180:181], v188 offset:0x2c00
	s_waitcnt lgkmcnt(6)
	s_nop 0
	v_mfma_f32_32x32x16_bf16 v[16:31], v[166:169], v[162:165], v[16:31]
	ds_read_b64_tr_b16 v[162:163], v188 offset:0x2600
	ds_read_b64_tr_b16 v[164:165], v188 offset:0x2e00
	s_waitcnt lgkmcnt(6)
	s_nop 0
	v_mfma_f32_32x32x16_bf16 v[64:79], v[132:135], v[170:173], v[64:79]
	ds_read_b64_tr_b16 v[166:167], v188 offset:0x3000
	ds_read_b64_tr_b16 v[168:169], v188 offset:0x3800
	s_waitcnt lgkmcnt(6)
	s_nop 0
	v_mfma_f32_32x32x16_bf16 v[48:63], v[132:135], v[174:177], v[48:63]
	ds_read_b64_tr_b16 v[170:171], v188 offset:0x3200
	ds_read_b64_tr_b16 v[172:173], v188 offset:0x3a00
	s_waitcnt lgkmcnt(6)
	s_nop 0
	v_mfma_f32_32x32x16_bf16 v[32:47], v[132:135], v[178:181], v[32:47]
	ds_read_b64_tr_b16 v[174:175], v188 offset:0x3400
	ds_read_b64_tr_b16 v[176:177], v188 offset:0x3c00
	s_waitcnt lgkmcnt(6)
	s_nop 0
	v_mfma_f32_32x32x16_bf16 v[16:31], v[132:135], v[162:165], v[16:31]
	ds_read_b64_tr_b16 v[132:133], v188 offset:0x3600
	ds_read_b64_tr_b16 v[134:135], v188 offset:0x3e00
	s_waitcnt lgkmcnt(6)
	s_nop 0
	v_mfma_f32_32x32x16_bf16 v[64:79], v[128:131], v[166:169], v[64:79]
	s_waitcnt lgkmcnt(4)
	s_nop 0
	v_mfma_f32_32x32x16_bf16 v[48:63], v[128:131], v[170:173], v[48:63]
	s_waitcnt lgkmcnt(2)
	s_nop 0
	v_mfma_f32_32x32x16_bf16 v[32:47], v[128:131], v[174:177], v[32:47]
	s_waitcnt lgkmcnt(0)
	s_nop 0
	v_mfma_f32_32x32x16_bf16 v[16:31], v[128:131], v[132:135], v[16:31]
	v_lshl_add_u64 v[144:145], v[144:145], 0, s[28:29]
	v_lshl_add_u64 v[146:147], v[146:147], 0, s[28:29]
	v_lshl_add_u64 v[148:149], v[148:149], 0, s[28:29]
	s_waitcnt vmcnt(0)
	s_add_u32 s44, s44, 0x10000
	s_waitcnt lgkmcnt(0)
	s_barrier
	s_addc_u32 s45, s45, 0
	s_cmp_eq_u32 s44, 0x7f0000
	s_cbranch_scc1 .LBB0_662

; __device__ __forceinline__ float vmax3(float x, float y, float z) { float r; asm("v_max3_f32 %0, %1, %2, %3" : "=v"(r) : "v"(x), "v"(y), "v"(z)); return r; }
; __device__ __forceinline__ float vmax2(float x, float y) { float r; asm("v_max_f32 %0, %1, %2" : "=v"(r) : "v"(x), "v"(y)); return r; }
; __device__ __forceinline__ void smax_tile(f32x16& p0, f32x16& p1, float& mhat, float& l_reg, f32x16 (&o)[4], float* al_l, const bool first, int r32, int hi,
;                                           bf16x8& pa0, bf16x8& pa1, bf16x8& pa2, bf16x8& pa3) {
;     float a = vmax3(p0[0], p0[1], p1[0]), b = vmax3(p0[2], p0[3], p1[1]); a = vmax3(a, p1[2], p1[3]);
; #pragma unroll
;     for (int r = 4; r < 16; r += 4) { a = vmax3(a, p0[r], p0[r + 1]); b = vmax3(b, p0[r + 2], p0[r + 3]); a = vmax3(a, p1[r], p1[r + 1]); b = vmax3(b, p1[r + 2], p1[r + 3]); }
;     float rm = vmax2(a, b);
;     { auto rr = __builtin_amdgcn_permlane32_swap(__float_as_uint(rm), __float_as_uint(rm), false, false); rm = vmax2(__uint_as_float(rr[0]), __uint_as_float(rr[1])); }
;     if (__builtin_expect(first || __any(rm > THRL), 0)) {
.LBB0_654:
	s_add_i32 s46, s86, 1
	s_cmp_lg_u32 s86, 2
	s_cselect_b32 s86, s46, 0
	s_lshl_b32 s87, s86, 14
	s_add_i32 s46, s68, s87
	s_add_i32 m0, s46, 0x6000
	v_max3_f32 v128, v96, v97, v80
	global_load_lds_dwordx4 v[146:147], off
	s_add_i32 m0, s46, 0x6400
	v_max3_f32 v129, v98, v99, v81
	global_load_lds_dwordx4 v[148:149], off
	v_max3_f32 v128, v128, v82, v83
	v_max3_f32 v129, v129, v102, v103
	v_max3_f32 v128, v128, v100, v101
	v_max3_f32 v129, v129, v86, v87
	v_max3_f32 v128, v128, v84, v85
	v_max3_f32 v129, v129, v106, v107
	v_max3_f32 v128, v128, v104, v105
	v_max3_f32 v129, v129, v90, v91
	v_max3_f32 v128, v128, v88, v89
	v_max3_f32 v129, v129, v110, v111
	v_max3_f32 v128, v128, v108, v109
	v_max3_f32 v129, v129, v94, v95
	v_max3_f32 v128, v128, v92, v93
	v_max_f32 v128, v128, v129
	s_addk_i32 s87, 0xc000
	s_cmp_eq_u32 s44, 0
	s_cbranch_scc1 .Lmy_dh_first
	v_cmp_lt_f32_e32 vcc, s79, v128
	s_cbranch_vccz .LBB0_651
	v_mov_b32_e32 v129, v128
	s_nop 1
	v_permlane32_swap_b32_e32 v128, v129
	v_max_f32_e32 v128, v128, v129
	s_branch .LBB0_660

; __device__ __forceinline__ float vmax2(float x, float y) { float r; asm("v_max_f32 %0, %1, %2" : "=v"(r) : "v"(x), "v"(y)); return r; }
; __device__ __forceinline__ void smax_tile(f32x16& p0, f32x16& p1, float& mhat, float& l_reg, f32x16 (&o)[4], float* al_l, const bool first, int r32, int hi,
;                                           bf16x8& pa0, bf16x8& pa1, bf16x8& pa2, bf16x8& pa3) {
;     ...
;     { auto rr = __builtin_amdgcn_permlane32_swap(__float_as_uint(rm), __float_as_uint(rm), false, false); rm = vmax2(__uint_as_float(rr[0]), __uint_as_float(rr[1])); }
;     if (__builtin_expect(first || __any(rm > THRL), 0)) {
.Lmy_dh_first:
	v_mov_b32_e32 v129, v128
	s_nop 1
	v_permlane32_swap_b32_e32 v128, v129
	v_max_f32_e32 v128, v128, v129
	s_branch .LBB0_661

; #define PK4(P, BASE, OUT) do { u32x4 w = {cvtpk(P[BASE + 0], P[BASE + 1]), cvtpk(P[BASE + 2], P[BASE + 3]), cvtpk(P[BASE + 4], P[BASE + 5]), cvtpk(P[BASE + 6], P[BASE + 7])}; \
;     OUT = *reinterpret_cast<bf16x8*>(&w); } while (0)
; #define DMA_KP(KB, tile, b) do { _Pragma("unroll") for (int _j = 0; _j < NKW; ++_j) glds16((const char*)(KB) + (size_t)(tile) * (KVBLK * LDK * 2) + koff[_j], (LAS unsigned*)(ldsL + (b) * SHM_K + (wid * NKW + _j) * 1024)); } while (0)
; #define DMA_VP(VB, tile, b) do { _Pragma("unroll") for (int _j = 0; _j < 2; ++_j) glds16((const char*)(VB) + (size_t)(tile) * (KVBLK * LDV * 2) + voff[_j], (LAS unsigned*)(ldsL + 3 * SHM_K + (b) * SHM_V + (wid * 2 + _j) * 1024)); } while (0)
; __device__ __forceinline__ void smax_tile(f32x16& p0, f32x16& p1, float& mhat, float& l_reg, f32x16 (&o)[4], float* al_l, const bool first, int r32, int hi,
;                                           bf16x8& pa0, bf16x8& pa1, bf16x8& pa2, bf16x8& pa3) {
;     ...
; #pragma unroll
;     for (int r = 0; r < 16; ++r) p0[r] = __builtin_amdgcn_exp2f(p0[r]);
; #pragma unroll
;     for (int r = 0; r < 16; ++r) p1[r] = __builtin_amdgcn_exp2f(p1[r]);
;     float ps = p0[0];
; #pragma unroll
;     for (int r = 1; r < 16; ++r) ps += p0[r];
; #pragma unroll
;     for (int r = 0; r < 16; ++r) ps += p1[r];
;     { auto rr = __builtin_amdgcn_permlane32_swap(__float_as_uint(ps), __float_as_uint(ps), false, false); ps = __uint_as_float(rr[0]) + __uint_as_float(rr[1]); }
;     l_reg += ps;
;     ...
;     PK4(p0, 0, pa0); PK4(p0, 8, pa1); PK4(p1, 0, pa2); PK4(p1, 8, pa3);
;     ...
;     if (nxt_ && g == 1) { DMA_KP(nKh, 0, 0); DMA_KP(nKh, 1, 1); DMA_VP(nVh, 0, 0); TOUCH_Q(); }
;     SEG_S(NT - 1);
;     if (nxt_ && g == 0) { DMA_KP(nKh, 0, 0); DMA_KP(nKh, 1, 1); DMA_VP(nVh, 0, 0); TOUCH_Q(); }
.LBB0_667:
	v_exp_f32_e32 v96, v96
	v_exp_f32_e32 v97, v97
	v_exp_f32_e32 v98, v98
	v_exp_f32_e32 v99, v99
	v_exp_f32_e32 v100, v100
	v_exp_f32_e32 v101, v101
	v_exp_f32_e32 v121, v108
	v_add_f32_e32 v108, v97, v96
	v_exp_f32_e32 v102, v102
	v_add_f32_e32 v108, v98, v108
	v_exp_f32_e32 v103, v103
	v_add_f32_e32 v108, v99, v108
	v_exp_f32_e32 v104, v104
	v_add_f32_e32 v108, v100, v108
	v_exp_f32_e32 v105, v105
	v_add_f32_e32 v108, v101, v108
	v_exp_f32_e32 v106, v106
	v_add_f32_e32 v108, v102, v108
	v_exp_f32_e32 v107, v107
	v_add_f32_e32 v108, v103, v108
	v_add_f32_e32 v108, v104, v108
	v_exp_f32_e32 v122, v109
	v_add_f32_e32 v108, v105, v108
	v_exp_f32_e32 v123, v110
	v_add_f32_e32 v108, v106, v108
	v_exp_f32_e32 v124, v111
	v_add_f32_e32 v108, v107, v108
	v_exp_f32_e32 v80, v80
	v_add_f32_e32 v108, v121, v108
	v_exp_f32_e32 v81, v81
	v_add_f32_e32 v108, v122, v108
	v_exp_f32_e32 v82, v82
	v_add_f32_e32 v108, v123, v108
	v_exp_f32_e32 v83, v83
	v_add_f32_e32 v108, v124, v108
	v_exp_f32_e32 v84, v84
	v_add_f32_e32 v108, v80, v108
	v_exp_f32_e32 v85, v85
	v_add_f32_e32 v108, v81, v108
	v_exp_f32_e32 v86, v86
	v_add_f32_e32 v108, v82, v108
	v_exp_f32_e32 v87, v87
	v_add_f32_e32 v108, v83, v108
	v_exp_f32_e32 v88, v88
	v_add_f32_e32 v108, v84, v108
	v_exp_f32_e32 v89, v89
	v_add_f32_e32 v108, v85, v108
	v_exp_f32_e32 v90, v90
	v_add_f32_e32 v108, v86, v108
	v_exp_f32_e32 v91, v91
	v_add_f32_e32 v108, v87, v108
	v_exp_f32_e32 v92, v92
	v_add_f32_e32 v108, v88, v108
	v_exp_f32_e32 v93, v93
	v_add_f32_e32 v108, v89, v108
	v_exp_f32_e32 v94, v94
	v_add_f32_e32 v108, v90, v108
	v_exp_f32_e32 v95, v95
	v_add_f32_e32 v108, v91, v108
	v_add_f32_e32 v108, v92, v108
	v_add_f32_e32 v108, v93, v108
	v_add_f32_e32 v108, v94, v108
	v_add_f32_e32 v108, v95, v108
	v_add_f32_e32 v120, v159, v108
	v_cvt_pk_bf16_f32 v108, v96, v97
	v_cvt_pk_bf16_f32 v109, v98, v99
	v_cvt_pk_bf16_f32 v110, v100, v101
	v_cvt_pk_bf16_f32 v111, v102, v103
	v_cvt_pk_bf16_f32 v104, v104, v105
	v_cvt_pk_bf16_f32 v105, v106, v107
	v_cvt_pk_bf16_f32 v106, v121, v122
	v_cvt_pk_bf16_f32 v107, v123, v124
	v_cvt_pk_bf16_f32 v100, v80, v81
	v_cvt_pk_bf16_f32 v101, v82, v83
	v_cvt_pk_bf16_f32 v102, v84, v85
	v_cvt_pk_bf16_f32 v103, v86, v87
	v_cvt_pk_bf16_f32 v96, v88, v89
	v_cvt_pk_bf16_f32 v97, v90, v91
	v_cvt_pk_bf16_f32 v98, v92, v93
	v_cvt_pk_bf16_f32 v99, v94, v95
	s_cmp_eq_u32 s85, 0
	s_cselect_b64 s[12:13], -1, 0
	s_waitcnt lgkmcnt(0)
	s_barrier
	s_and_b64 s[38:39], s[44:45], s[12:13]
	s_andn2_b64 vcc, exec, s[38:39]
	s_cbranch_vccnz .LBB0_671
	s_mov_b32 m0, s69
	s_cmp_lg_u64 s[36:37], 0
	global_load_lds_dwordx4 v[116:117], off
	s_mov_b32 m0, s76
	s_cselect_b64 s[38:39], -1, 0
	global_load_lds_dwordx4 v[118:119], off
	s_mov_b32 m0, s77
	v_cmp_gt_i32_e32 vcc, 32, v156
	global_load_lds_dwordx4 v[114:115], off
	s_mov_b32 m0, s78
	s_and_b64 s[42:43], s[38:39], vcc
	global_load_lds_dwordx4 v[112:113], off
	s_and_saveexec_b64 s[38:39], s[42:43]
	s_cbranch_execz .LBB0_670
	v_add_u32_e32 v80, s57, v156
	v_ashrrev_i32_e32 v81, 31, v80
	v_lshlrev_b64 v[80:81], 10, v[80:81]
	v_lshl_add_u64 v[80:81], s[36:37], 0, v[80:81]
	s_add_i32 s36, s5, 0
	s_add_i32 m0, s36, 0x13000
	s_nop 0
	global_load_lds_dword v[80:81], off

; #define SBAR() __builtin_amdgcn_sched_barrier(0)
; #define LWN1(a) do { if constexpr (NW == 0) LW1(0, a); else if constexpr (NW == 1) LW1(1, a); else if constexpr (NW == 2) LW1(2, a); else if constexpr (NW == 3) LW1(3, a); else if constexpr (NW == 4) LW1(4, a); else if constexpr (NW == 5) LW1(5, a); else LW1(6, a); } while (0)
; #define LWN2(a, b) do { if constexpr (NW == 0) LW2(0, a, b); else if constexpr (NW == 1) LW2(1, a, b); else if constexpr (NW == 2) LW2(2, a, b); else if constexpr (NW == 3) LW2(3, a, b); else if constexpr (NW == 4) LW2(4, a, b); else if constexpr (NW == 5) LW2(5, a, b); else LW2(6, a, b); } while (0)
; __device__ __forceinline__ void smax_tile(f32x16& p0, f32x16& p1, float& mhat, float& l_reg, f32x16 (&o)[4], float* al_l, const bool first, int r32, int hi,
;                                           bf16x8& pa0, bf16x8& pa1, bf16x8& pa2, bf16x8& pa3) {
;     ...
;     { auto rr = __builtin_amdgcn_permlane32_swap(__float_as_uint(ps), __float_as_uint(ps), false, false); ps = __uint_as_float(rr[0]) + __uint_as_float(rr[1]); }
;     l_reg += ps;
; template <int DQK, bool HASQK, bool HASPV, int J> ...
;     constexpr int NQS = HASQK ? 2 * (DQK / 16) : 0, NS = NQS + (HASPV ? 16 : 0);
;     if constexpr (J < NS) {
;         constexpr int rd1 = (J + 1 < NS) ? ((J + 1 < NQS) ? 1 : 2) : 0, rd2 = (J + 2 < NS) ? ((J + 2 < NQS) ? 1 : 2) : 0, rd3 = (J + 3 < NS) ? ((J + 3 < NQS) ? 1 : 2) : 0, NW = rd1 + rd2 + rd3;
;     ...
;         if constexpr (J < NQS) { constexpr int d0 = J >> 1, h = J & 1;
;             LWN1(kf[d0][h]); SBAR();
;             if constexpr (h == 0) p0 = __builtin_amdgcn_mfma_f32_32x32x16_bf16(kf[d0][0], qr[d0], (d0 == 0) ? negm : p0, 0, 0, 0);
;             else p1 = __builtin_amdgcn_mfma_f32_32x32x16_bf16(kf[d0][1], qr[d0], (d0 == 0) ? negm : p1, 0, 0, 0);
;         } else { constexpr int q = J - NQS, g = q >> 2, d = q & 3;
;             LWN2(vf[g][2 * d], vf[g][2 * d + 1]); SBAR();
;             o[d] = __builtin_amdgcn_mfma_f32_32x32x16_bf16(pa[g], (bf16x8){vf[g][2 * d][0], vf[g][2 * d][1], vf[g][2 * d][2], vf[g][2 * d][3], vf[g][2 * d + 1][0], vf[g][2 * d + 1][1], vf[g][2 * d + 1][2], vf[g][2 * d + 1][3]}, o[d], 0, 0, 0);
;         }
;     ...
;         SBAR();
;         slot_read<DQK, HASQK, HASPV, J + 4>(kf, vf, ka_, vb_);
;         SBAR();
;         slot_run<DQK, HASQK, HASPV, J + 1>(kf, vf, ka_, vb_, qr, p0, p1, negm, o, pa);
.LBB0_671:
	s_add_i32 s36, s86, 1
	s_cmp_lg_u32 s86, 2
	s_cselect_b32 s36, s36, 0
	s_lshl_b32 s37, s36, 14
	s_addk_i32 s37, 0xc000
	s_cmp_lg_u32 s36, 0
	s_cselect_b32 s36, s37, 0x8000
	v_add_u32_e32 v121, s36, v157
	ds_read_b64_tr_b16 v[112:113], v121 offset:0
	ds_read_b64_tr_b16 v[114:115], v121 offset:0x800
	ds_read_b64_tr_b16 v[116:117], v121 offset:0x200
	ds_read_b64_tr_b16 v[118:119], v121 offset:0xa00
	ds_read_b64_tr_b16 v[122:123], v121 offset:0x400
	ds_read_b64_tr_b16 v[124:125], v121 offset:0xc00
	ds_read_b64_tr_b16 v[126:127], v121 offset:0x600
	ds_read_b64_tr_b16 v[128:129], v121 offset:0xe00
	v_xor_b32_e32 v80, 0x80000000, v158
	v_mov_b32_e32 v81, v80
	v_mov_b32_e32 v82, v80
	v_mov_b32_e32 v83, v80
	v_mov_b32_e32 v84, v80
	v_mov_b32_e32 v85, v80
	v_mov_b32_e32 v86, v80
	v_mov_b32_e32 v87, v80
	v_mov_b32_e32 v88, v80
	v_mov_b32_e32 v89, v80
	v_mov_b32_e32 v90, v80
	v_mov_b32_e32 v91, v80
	v_mov_b32_e32 v92, v80
	v_mov_b32_e32 v93, v80
	v_mov_b32_e32 v94, v80
	v_mov_b32_e32 v95, v80
	s_waitcnt lgkmcnt(6)
	s_nop 0
	v_mfma_f32_32x32x16_bf16 v[64:79], v[108:111], v[112:115], v[64:79]
	ds_read_b64_tr_b16 v[80:81], v121 offset:0x1000
	ds_read_b64_tr_b16 v[82:83], v121 offset:0x1800
	s_waitcnt lgkmcnt(6)
	s_nop 0
	v_mfma_f32_32x32x16_bf16 v[48:63], v[108:111], v[116:119], v[48:63]
	ds_read_b64_tr_b16 v[84:85], v121 offset:0x1200
	ds_read_b64_tr_b16 v[86:87], v121 offset:0x1a00
	s_waitcnt lgkmcnt(6)
	s_nop 0
	v_mfma_f32_32x32x16_bf16 v[32:47], v[108:111], v[122:125], v[32:47]
	ds_read_b64_tr_b16 v[88:89], v121 offset:0x1400
	ds_read_b64_tr_b16 v[90:91], v121 offset:0x1c00
	s_waitcnt lgkmcnt(6)
	s_nop 0
	v_mfma_f32_32x32x16_bf16 v[16:31], v[108:111], v[126:129], v[16:31]
	ds_read_b64_tr_b16 v[92:93], v121 offset:0x1600
	ds_read_b64_tr_b16 v[94:95], v121 offset:0x1e00
	s_waitcnt lgkmcnt(6)
	s_nop 0
	v_mfma_f32_32x32x16_bf16 v[64:79], v[104:107], v[80:83], v[64:79]
	ds_read_b64_tr_b16 v[80:81], v121 offset:0x2000
	ds_read_b64_tr_b16 v[82:83], v121 offset:0x2800
	s_waitcnt lgkmcnt(6)
	s_nop 0
	v_mfma_f32_32x32x16_bf16 v[48:63], v[104:107], v[84:87], v[48:63]
	ds_read_b64_tr_b16 v[84:85], v121 offset:0x2200
	ds_read_b64_tr_b16 v[86:87], v121 offset:0x2a00
	s_waitcnt lgkmcnt(6)
	s_nop 0
	v_mfma_f32_32x32x16_bf16 v[32:47], v[104:107], v[88:91], v[32:47]
	ds_read_b64_tr_b16 v[88:89], v121 offset:0x2400
	ds_read_b64_tr_b16 v[90:91], v121 offset:0x2c00
	s_waitcnt lgkmcnt(6)
	s_nop 0
	v_mfma_f32_32x32x16_bf16 v[16:31], v[104:107], v[92:95], v[16:31]
	ds_read_b64_tr_b16 v[92:93], v121 offset:0x2600
	ds_read_b64_tr_b16 v[94:95], v121 offset:0x2e00
	s_waitcnt lgkmcnt(6)
	s_nop 0
	v_mfma_f32_32x32x16_bf16 v[64:79], v[100:103], v[80:83], v[64:79]
	ds_read_b64_tr_b16 v[80:81], v121 offset:0x3000
	ds_read_b64_tr_b16 v[82:83], v121 offset:0x3800
	s_waitcnt lgkmcnt(6)
	s_nop 0
	v_mfma_f32_32x32x16_bf16 v[48:63], v[100:103], v[84:87], v[48:63]
	ds_read_b64_tr_b16 v[84:85], v121 offset:0x3200
	ds_read_b64_tr_b16 v[86:87], v121 offset:0x3a00
	s_waitcnt lgkmcnt(6)
	s_nop 0
	v_mfma_f32_32x32x16_bf16 v[32:47], v[100:103], v[88:91], v[32:47]
	ds_read_b64_tr_b16 v[88:89], v121 offset:0x3400
	ds_read_b64_tr_b16 v[90:91], v121 offset:0x3c00
	s_waitcnt lgkmcnt(6)
	s_nop 0
	v_mfma_f32_32x32x16_bf16 v[16:31], v[100:103], v[92:95], v[16:31]
	ds_read_b64_tr_b16 v[92:93], v121 offset:0x3600
	ds_read_b64_tr_b16 v[94:95], v121 offset:0x3e00
	s_waitcnt lgkmcnt(6)
	s_nop 0
	v_mfma_f32_32x32x16_bf16 v[64:79], v[96:99], v[80:83], v[64:79]
	s_waitcnt lgkmcnt(4)
	s_nop 0
	v_mfma_f32_32x32x16_bf16 v[48:63], v[96:99], v[84:87], v[48:63]
	s_waitcnt lgkmcnt(2)
	s_nop 0
	v_mfma_f32_32x32x16_bf16 v[32:47], v[96:99], v[88:91], v[32:47]
	s_waitcnt lgkmcnt(0)
	s_nop 0
	v_mfma_f32_32x32x16_bf16 v[16:31], v[96:99], v[92:95], v[16:31]
	s_waitcnt lgkmcnt(0)
	s_barrier
	v_mov_b32_e32 v244, v120
	s_nop 1
	v_permlane32_swap_b32_e32 v120, v244
	v_add_f32_e32 v120, v120, v244
	s_andn2_b64 vcc, exec, s[12:13]
	s_cbranch_vccz .LBB0_676
	s_and_saveexec_b64 s[12:13], s[10:11]
